# proj K-loop LDS-DMA loads use SGPR base + 32-bit lane offset (no per-load 64-bit address arithmetic)
# speedup vs baseline: 1.0066x; 1.0066x over previous
.LBB0_235:
	s_add_u32 s4, s0, 0xfffe0080
	s_addc_u32 s5, s1, -1
	s_add_i32 s52, 0, 0x10000
	s_cmp_eq_u32 s51, 4
	s_cselect_b32 s7, s21, s5
	s_cselect_b32 s6, s29, s4
	s_cselect_b32 s5, s23, s50
	s_cselect_b32 s4, s48, s49
	s_add_i32 s53, 0, 0x14000
	ds_read_b128 v[20:23], v192
	ds_read_b128 v[24:27], v249
	ds_read_b128 v[28:31], v192 offset:2048
	ds_read_b128 v[32:35], v249 offset:2048
	ds_read_b128 v[4:7], v192 offset:16384
	ds_read_b128 v[8:11], v249 offset:16384
	ds_read_b128 v[12:15], v192 offset:18432
	ds_read_b128 v[16:19], v249 offset:18432
	s_add_i32 m0, s37, 0xc000
	ds_read_b128 v[184:187], v193
	ds_read_b128 v[188:191], v250
	ds_read_b128 v[194:197], v193 offset:2048
	ds_read_b128 v[198:201], v250 offset:2048
	ds_read_b128 v[202:205], v193 offset:4096
	ds_read_b128 v[206:209], v250 offset:4096
	ds_read_b128 v[226:229], v193 offset:6144
	ds_read_b128 v[230:233], v250 offset:6144
	global_load_lds_dwordx4 v180, s[0:1]
	s_add_i32 m0, s37, 0xe000
	s_nop 0
	global_load_lds_dwordx4 v182, s[0:1]
	s_waitcnt vmcnt(8)
	s_waitcnt lgkmcnt(0)
	s_barrier
	s_setprio 1
	s_waitcnt lgkmcnt(0)
	v_mfma_scale_f32_16x16x128_f8f6f4 v[96:99], v[20:27], v[184:191], v[96:99], v1, v1 op_sel_hi:[0,0,0]
	v_mfma_scale_f32_16x16x128_f8f6f4 v[92:95], v[28:35], v[184:191], v[92:95], v1, v1 op_sel_hi:[0,0,0]
	v_mfma_scale_f32_16x16x128_f8f6f4 v[88:91], v[20:27], v[194:201], v[88:91], v1, v1 op_sel_hi:[0,0,0]
	v_mfma_scale_f32_16x16x128_f8f6f4 v[84:87], v[28:35], v[194:201], v[84:87], v1, v1 op_sel_hi:[0,0,0]
	v_mfma_scale_f32_16x16x128_f8f6f4 v[80:83], v[20:27], v[202:209], v[80:83], v1, v1 op_sel_hi:[0,0,0]
	v_mfma_scale_f32_16x16x128_f8f6f4 v[76:79], v[28:35], v[202:209], v[76:79], v1, v1 op_sel_hi:[0,0,0]
	v_mfma_scale_f32_16x16x128_f8f6f4 v[72:75], v[20:27], v[226:233], v[72:75], v1, v1 op_sel_hi:[0,0,0]
	v_mfma_scale_f32_16x16x128_f8f6f4 v[68:71], v[28:35], v[226:233], v[68:71], v1, v1 op_sel_hi:[0,0,0]
	s_setprio 0
	s_setprio 1
	v_mfma_scale_f32_16x16x128_f8f6f4 v[160:163], v[4:11], v[184:191], v[160:163], v1, v1 op_sel_hi:[0,0,0]
	v_mfma_scale_f32_16x16x128_f8f6f4 v[156:159], v[12:19], v[184:191], v[156:159], v1, v1 op_sel_hi:[0,0,0]
	v_mfma_scale_f32_16x16x128_f8f6f4 v[152:155], v[4:11], v[194:201], v[152:155], v1, v1 op_sel_hi:[0,0,0]
	v_mfma_scale_f32_16x16x128_f8f6f4 v[148:151], v[12:19], v[194:201], v[148:151], v1, v1 op_sel_hi:[0,0,0]
	v_mfma_scale_f32_16x16x128_f8f6f4 v[144:147], v[4:11], v[202:209], v[144:147], v1, v1 op_sel_hi:[0,0,0]
	v_mfma_scale_f32_16x16x128_f8f6f4 v[140:143], v[12:19], v[202:209], v[140:143], v1, v1 op_sel_hi:[0,0,0]
	v_mfma_scale_f32_16x16x128_f8f6f4 v[136:139], v[4:11], v[226:233], v[136:139], v1, v1 op_sel_hi:[0,0,0]
	v_mfma_scale_f32_16x16x128_f8f6f4 v[132:135], v[12:19], v[226:233], v[132:135], v1, v1 op_sel_hi:[0,0,0]
	s_setprio 0
	s_barrier
	s_add_i32 s52, s52, s36
	s_mov_b32 m0, s52
	ds_read_b128 v[194:197], v193 offset:16384
	ds_read_b128 v[198:201], v250 offset:16384
	ds_read_b128 v[202:205], v193 offset:18432
	ds_read_b128 v[206:209], v250 offset:18432
	ds_read_b128 v[226:229], v193 offset:20480
	ds_read_b128 v[230:233], v250 offset:20480
	ds_read_b128 v[234:237], v193 offset:22528
	ds_read_b128 v[238:241], v250 offset:22528
	global_load_lds_dwordx4 v176, s[4:5]
	s_add_i32 m0, s52, 0x2000
	s_add_u32 s54, s4, 0x20000
	s_addc_u32 s55, s5, 0
	s_add_i32 s52, s53, s36
	global_load_lds_dwordx4 v172, s[4:5]
	s_mov_b32 m0, s52
	s_nop 0
	global_load_lds_dwordx4 v176, s[54:55]
	s_add_i32 m0, s52, 0x2000
	s_nop 0
	global_load_lds_dwordx4 v172, s[54:55]
	s_mov_b32 m0, s37
	s_nop 0
	global_load_lds_dwordx4 v178, s[6:7]
	s_mov_b32 m0, s38
	s_nop 0
	global_load_lds_dwordx4 v174, s[6:7]
	s_waitcnt vmcnt(8)
	s_waitcnt lgkmcnt(0)
	s_barrier
	s_setprio 1
	s_waitcnt lgkmcnt(0)
	v_mfma_scale_f32_16x16x128_f8f6f4 v[64:67], v[20:27], v[194:201], v[64:67], v1, v1 op_sel_hi:[0,0,0]
	v_mfma_scale_f32_16x16x128_f8f6f4 v[60:63], v[28:35], v[194:201], v[60:63], v1, v1 op_sel_hi:[0,0,0]
	v_mfma_scale_f32_16x16x128_f8f6f4 v[56:59], v[20:27], v[202:209], v[56:59], v1, v1 op_sel_hi:[0,0,0]
	v_mfma_scale_f32_16x16x128_f8f6f4 v[52:55], v[28:35], v[202:209], v[52:55], v1, v1 op_sel_hi:[0,0,0]
	v_mfma_scale_f32_16x16x128_f8f6f4 v[48:51], v[20:27], v[226:233], v[48:51], v1, v1 op_sel_hi:[0,0,0]
	v_mfma_scale_f32_16x16x128_f8f6f4 v[44:47], v[28:35], v[226:233], v[44:47], v1, v1 op_sel_hi:[0,0,0]
	v_mfma_scale_f32_16x16x128_f8f6f4 v[40:43], v[20:27], v[234:241], v[40:43], v1, v1 op_sel_hi:[0,0,0]
	v_mfma_scale_f32_16x16x128_f8f6f4 v[36:39], v[28:35], v[234:241], v[36:39], v1, v1 op_sel_hi:[0,0,0]
	s_setprio 0
	s_setprio 1
	v_mfma_scale_f32_16x16x128_f8f6f4 v[128:131], v[4:11], v[194:201], v[128:131], v1, v1 op_sel_hi:[0,0,0]
	v_mfma_scale_f32_16x16x128_f8f6f4 v[124:127], v[12:19], v[194:201], v[124:127], v1, v1 op_sel_hi:[0,0,0]
	v_mfma_scale_f32_16x16x128_f8f6f4 v[120:123], v[4:11], v[202:209], v[120:123], v1, v1 op_sel_hi:[0,0,0]
	v_mfma_scale_f32_16x16x128_f8f6f4 v[116:119], v[12:19], v[202:209], v[116:119], v1, v1 op_sel_hi:[0,0,0]
	v_mfma_scale_f32_16x16x128_f8f6f4 v[112:115], v[4:11], v[226:233], v[112:115], v1, v1 op_sel_hi:[0,0,0]
	v_mfma_scale_f32_16x16x128_f8f6f4 v[108:111], v[12:19], v[226:233], v[108:111], v1, v1 op_sel_hi:[0,0,0]
	v_mfma_scale_f32_16x16x128_f8f6f4 v[104:107], v[4:11], v[234:241], v[104:107], v1, v1 op_sel_hi:[0,0,0]
	v_mfma_scale_f32_16x16x128_f8f6f4 v[100:103], v[12:19], v[234:241], v[100:103], v1, v1 op_sel_hi:[0,0,0]
	s_setprio 0
	s_barrier
	s_add_i32 s52, 0, 0x18000
	s_add_i32 s53, 0, 0x1c000
	ds_read_b128 v[4:7], v192 offset:32768
	ds_read_b128 v[8:11], v249 offset:32768
	ds_read_b128 v[12:15], v192 offset:34816
	ds_read_b128 v[16:19], v249 offset:34816
	ds_read_b128 v[20:23], v192 offset:49152
	ds_read_b128 v[24:27], v249 offset:49152
	ds_read_b128 v[28:31], v192 offset:51200
	ds_read_b128 v[32:35], v249 offset:51200
	s_add_u32 s6, s6, 0x20000
	s_addc_u32 s7, s7, 0
	s_mov_b32 m0, s39
	ds_read_b128 v[194:197], v193 offset:32768
	ds_read_b128 v[198:201], v250 offset:32768
	ds_read_b128 v[202:205], v193 offset:34816
	ds_read_b128 v[206:209], v250 offset:34816
	ds_read_b128 v[226:229], v193 offset:36864
	ds_read_b128 v[230:233], v250 offset:36864
	ds_read_b128 v[234:237], v193 offset:38912
	ds_read_b128 v[238:241], v250 offset:38912
	global_load_lds_dwordx4 v178, s[6:7]
	s_mov_b32 m0, s42
	s_nop 0
	global_load_lds_dwordx4 v174, s[6:7]
	s_waitcnt vmcnt(8)
	s_waitcnt lgkmcnt(0)
	s_barrier
	s_setprio 1
	s_waitcnt lgkmcnt(0)
	v_mfma_scale_f32_16x16x128_f8f6f4 v[96:99], v[4:11], v[194:201], v[96:99], v1, v1 op_sel_hi:[0,0,0]
	v_mfma_scale_f32_16x16x128_f8f6f4 v[92:95], v[12:19], v[194:201], v[92:95], v1, v1 op_sel_hi:[0,0,0]
	v_mfma_scale_f32_16x16x128_f8f6f4 v[88:91], v[4:11], v[202:209], v[88:91], v1, v1 op_sel_hi:[0,0,0]
	v_mfma_scale_f32_16x16x128_f8f6f4 v[84:87], v[12:19], v[202:209], v[84:87], v1, v1 op_sel_hi:[0,0,0]
	v_mfma_scale_f32_16x16x128_f8f6f4 v[80:83], v[4:11], v[226:233], v[80:83], v1, v1 op_sel_hi:[0,0,0]
	v_mfma_scale_f32_16x16x128_f8f6f4 v[76:79], v[12:19], v[226:233], v[76:79], v1, v1 op_sel_hi:[0,0,0]
	v_mfma_scale_f32_16x16x128_f8f6f4 v[72:75], v[4:11], v[234:241], v[72:75], v1, v1 op_sel_hi:[0,0,0]
	v_mfma_scale_f32_16x16x128_f8f6f4 v[68:71], v[12:19], v[234:241], v[68:71], v1, v1 op_sel_hi:[0,0,0]
	s_setprio 0
	s_setprio 1
	v_mfma_scale_f32_16x16x128_f8f6f4 v[160:163], v[20:27], v[194:201], v[160:163], v1, v1 op_sel_hi:[0,0,0]
	v_mfma_scale_f32_16x16x128_f8f6f4 v[156:159], v[28:35], v[194:201], v[156:159], v1, v1 op_sel_hi:[0,0,0]
	v_mfma_scale_f32_16x16x128_f8f6f4 v[152:155], v[20:27], v[202:209], v[152:155], v1, v1 op_sel_hi:[0,0,0]
	v_mfma_scale_f32_16x16x128_f8f6f4 v[148:151], v[28:35], v[202:209], v[148:151], v1, v1 op_sel_hi:[0,0,0]
	v_mfma_scale_f32_16x16x128_f8f6f4 v[144:147], v[20:27], v[226:233], v[144:147], v1, v1 op_sel_hi:[0,0,0]
	v_mfma_scale_f32_16x16x128_f8f6f4 v[140:143], v[28:35], v[226:233], v[140:143], v1, v1 op_sel_hi:[0,0,0]
	v_mfma_scale_f32_16x16x128_f8f6f4 v[136:139], v[20:27], v[234:241], v[136:139], v1, v1 op_sel_hi:[0,0,0]
	v_mfma_scale_f32_16x16x128_f8f6f4 v[132:135], v[28:35], v[234:241], v[132:135], v1, v1 op_sel_hi:[0,0,0]
	s_setprio 0
	s_barrier
	s_add_u32 s58, s4, 0x80
	s_addc_u32 s59, s5, 0
	s_add_u32 s62, s6, 0xfffe0080
	s_addc_u32 s63, s7, -1
	s_add_i32 s6, s52, s36
	s_mov_b32 m0, s6
	ds_read_b128 v[194:197], v193 offset:49152
	ds_read_b128 v[198:201], v250 offset:49152
	ds_read_b128 v[202:205], v193 offset:51200
	ds_read_b128 v[206:209], v250 offset:51200
	ds_read_b128 v[226:229], v193 offset:53248
	ds_read_b128 v[230:233], v250 offset:53248
	ds_read_b128 v[234:237], v193 offset:55296
	ds_read_b128 v[238:241], v250 offset:55296
	global_load_lds_dwordx4 v176, s[58:59]
	s_add_i32 m0, s6, 0x2000
	s_add_u32 s4, s4, 0x20080
	s_addc_u32 s5, s5, 0
	s_add_i32 s6, s53, s36
	global_load_lds_dwordx4 v172, s[58:59]
	s_mov_b32 m0, s6
	s_nop 0
	global_load_lds_dwordx4 v176, s[4:5]
	s_add_i32 m0, s6, 0x2000
	s_nop 0
	global_load_lds_dwordx4 v172, s[4:5]
	s_mov_b32 m0, s45
	s_nop 0
	global_load_lds_dwordx4 v178, s[62:63]
	s_mov_b32 m0, s46
	s_nop 0
	global_load_lds_dwordx4 v174, s[62:63]
	s_waitcnt vmcnt(8)
	s_waitcnt lgkmcnt(0)
	s_barrier
	s_setprio 1
	s_waitcnt lgkmcnt(0)
	v_mfma_scale_f32_16x16x128_f8f6f4 v[64:67], v[4:11], v[194:201], v[64:67], v1, v1 op_sel_hi:[0,0,0]
	v_mfma_scale_f32_16x16x128_f8f6f4 v[60:63], v[12:19], v[194:201], v[60:63], v1, v1 op_sel_hi:[0,0,0]
	v_mfma_scale_f32_16x16x128_f8f6f4 v[56:59], v[4:11], v[202:209], v[56:59], v1, v1 op_sel_hi:[0,0,0]
	v_mfma_scale_f32_16x16x128_f8f6f4 v[52:55], v[12:19], v[202:209], v[52:55], v1, v1 op_sel_hi:[0,0,0]
	v_mfma_scale_f32_16x16x128_f8f6f4 v[48:51], v[4:11], v[226:233], v[48:51], v1, v1 op_sel_hi:[0,0,0]
	v_mfma_scale_f32_16x16x128_f8f6f4 v[44:47], v[12:19], v[226:233], v[44:47], v1, v1 op_sel_hi:[0,0,0]
	v_mfma_scale_f32_16x16x128_f8f6f4 v[40:43], v[4:11], v[234:241], v[40:43], v1, v1 op_sel_hi:[0,0,0]
	v_mfma_scale_f32_16x16x128_f8f6f4 v[36:39], v[12:19], v[234:241], v[36:39], v1, v1 op_sel_hi:[0,0,0]
	s_setprio 0
	s_setprio 1
	v_mfma_scale_f32_16x16x128_f8f6f4 v[128:131], v[20:27], v[194:201], v[128:131], v1, v1 op_sel_hi:[0,0,0]
	v_mfma_scale_f32_16x16x128_f8f6f4 v[124:127], v[28:35], v[194:201], v[124:127], v1, v1 op_sel_hi:[0,0,0]
	v_mfma_scale_f32_16x16x128_f8f6f4 v[120:123], v[20:27], v[202:209], v[120:123], v1, v1 op_sel_hi:[0,0,0]
	v_mfma_scale_f32_16x16x128_f8f6f4 v[116:119], v[28:35], v[202:209], v[116:119], v1, v1 op_sel_hi:[0,0,0]
	v_mfma_scale_f32_16x16x128_f8f6f4 v[112:115], v[20:27], v[226:233], v[112:115], v1, v1 op_sel_hi:[0,0,0]
	v_mfma_scale_f32_16x16x128_f8f6f4 v[108:111], v[28:35], v[226:233], v[108:111], v1, v1 op_sel_hi:[0,0,0]
	v_mfma_scale_f32_16x16x128_f8f6f4 v[104:107], v[20:27], v[234:241], v[104:107], v1, v1 op_sel_hi:[0,0,0]
	v_mfma_scale_f32_16x16x128_f8f6f4 v[100:103], v[28:35], v[234:241], v[100:103], v1, v1 op_sel_hi:[0,0,0]
	s_setprio 0
	s_barrier
	s_add_i32 s51, s51, 2
	s_add_u32 s0, s0, 0x100
	s_addc_u32 s1, s1, 0
	s_add_u32 s49, s49, 0x100
	s_addc_u32 s50, s50, 0
	s_cmp_gt_u32 s51, 5
	s_cbranch_scc0 .LBB0_235
	s_and_b64 vcc, exec, s[18:19]
	s_cbranch_vccz .LBB0_238
	s_barrier
